# v46: v41 + load de-serialisation: norm-phase modulation vectors (2 paths) and MoE gather expert-count prefix loads issued together, one wait
# speedup vs baseline: 1.0116x; 1.0116x over previous
.LBB0_633:
	s_and_b64 vcc, exec, s[6:7]
	s_cbranch_vccz .LBB0_651
	s_load_dwordx2 s[6:7], s[2:3], 0x28
	v_readlane_b32 s8, v255, 2
	v_readlane_b32 s9, v255, 3
	s_lshl_b32 s94, s8, 10
	s_lshl_b64 s[8:9], s[94:95], 2
	s_waitcnt lgkmcnt(0)
	s_add_u32 s6, s6, s8
	s_addc_u32 s7, s7, s9
	s_lshl_b32 s8, s36, 6
	v_readlane_b32 s9, v254, 9
	s_add_i32 s22, s8, s9
	s_ashr_i32 s8, s22, 11
	s_mul_hi_i32 s9, s8, 0x6000
	s_mulk_i32 s8, 0x6000
	s_waitcnt vmcnt(0)
	v_mbcnt_lo_u32_b32 v0, -1, 0
	v_mbcnt_hi_u32_b32 v0, -1, v0
	s_add_u32 s8, s34, s8
	v_and_b32_e32 v0, 63, v0
	s_addc_u32 s9, s35, s9
	s_add_u32 s10, s8, 0x1000
	v_lshlrev_b32_e32 v36, 4, v0
	s_addc_u32 s11, s9, 0
	global_load_dwordx4 v[142:145], v36, s[6:7]
	global_load_dwordx4 v[146:149], v36, s[10:11]
	v_or_b32_e32 v10, 0x400, v36
	v_or_b32_e32 v14, 0x800, v36
	v_or_b32_e32 v30, 0xc00, v36
	global_load_dwordx4 v[2:5], v36, s[8:9]
	global_load_dwordx4 v[150:153], v36, s[6:7] offset:1024
	s_nop 0
	global_load_dwordx4 v[154:157], v10, s[10:11]
	global_load_dwordx4 v[6:9], v36, s[8:9] offset:1024
	global_load_dwordx4 v[158:161], v36, s[6:7] offset:2048
	s_nop 0
	global_load_dwordx4 v[162:165], v14, s[10:11]
	global_load_dwordx4 v[166:169], v36, s[6:7] offset:3072
	s_nop 0
	global_load_dwordx4 v[170:173], v30, s[10:11]
	global_load_dwordx4 v[10:13], v36, s[8:9] offset:2048
	global_load_dwordx4 v[14:17], v36, s[8:9] offset:3072
	s_ashr_i32 s23, s22, 31
	s_or_b32 s20, s22, 1
	s_ashr_i32 s21, s20, 31
	s_or_b32 s18, s22, 2
	s_ashr_i32 s19, s18, 31
	s_or_b32 s16, s22, 3
	s_ashr_i32 s17, s16, 31
	s_or_b32 s14, s22, 4
	s_ashr_i32 s15, s14, 31
	s_or_b32 s12, s22, 5
	s_ashr_i32 s13, s12, 31
	s_or_b32 s10, s22, 6
	s_ashr_i32 s11, s10, 31
	v_cmp_eq_u32_e64 s[6:7], 0, v0
	v_lshlrev_b32_e32 v34, 3, v0
	v_mov_b32_e32 v35, v1
	v_lshl_add_u64 v[34:35], s[4:5], 0, v[34:35]
	s_lshl_b64 s[4:5], s[22:23], 11
	v_lshl_add_u64 v[36:37], v[34:35], 0, s[4:5]
	global_load_dwordx2 v[94:95], v[36:37], off
	global_load_dwordx2 v[90:91], v[36:37], off offset:512
	global_load_dwordx2 v[92:93], v[36:37], off offset:1024
	global_load_dwordx2 v[96:97], v[36:37], off offset:1536
	s_lshl_b64 s[4:5], s[20:21], 11
	v_lshl_add_u64 v[36:37], v[34:35], 0, s[4:5]
	s_lshl_b64 s[4:5], s[18:19], 11
	global_load_dwordx2 v[88:89], v[36:37], off
	global_load_dwordx2 v[86:87], v[36:37], off offset:512
	global_load_dwordx2 v[84:85], v[36:37], off offset:1024
	global_load_dwordx2 v[82:83], v[36:37], off offset:1536
	v_lshl_add_u64 v[36:37], v[34:35], 0, s[4:5]
	s_lshl_b64 s[4:5], s[16:17], 11
	global_load_dwordx2 v[80:81], v[36:37], off
	global_load_dwordx2 v[78:79], v[36:37], off offset:512
	global_load_dwordx2 v[76:77], v[36:37], off offset:1024
	global_load_dwordx2 v[74:75], v[36:37], off offset:1536
	v_lshl_add_u64 v[36:37], v[34:35], 0, s[4:5]
	s_lshl_b64 s[4:5], s[14:15], 11
	global_load_dwordx2 v[72:73], v[36:37], off
	global_load_dwordx2 v[70:71], v[36:37], off offset:512
	global_load_dwordx2 v[68:69], v[36:37], off offset:1024
	global_load_dwordx2 v[66:67], v[36:37], off offset:1536
	v_lshl_add_u64 v[36:37], v[34:35], 0, s[4:5]
	s_lshl_b64 s[4:5], s[12:13], 11
	global_load_dwordx2 v[64:65], v[36:37], off
	global_load_dwordx2 v[62:63], v[36:37], off offset:512
	global_load_dwordx2 v[60:61], v[36:37], off offset:1024
	global_load_dwordx2 v[58:59], v[36:37], off offset:1536
	v_lshl_add_u64 v[36:37], v[34:35], 0, s[4:5]
	s_lshl_b64 s[4:5], s[10:11], 11
	global_load_dwordx2 v[56:57], v[36:37], off
	global_load_dwordx2 v[54:55], v[36:37], off offset:512
	global_load_dwordx2 v[52:53], v[36:37], off offset:1024
	global_load_dwordx2 v[50:51], v[36:37], off offset:1536
	v_lshl_add_u64 v[36:37], v[34:35], 0, s[4:5]
	s_or_b32 s4, s22, 7
	s_ashr_i32 s5, s4, 31
	s_lshl_b64 s[8:9], s[4:5], 11
	v_lshl_add_u64 v[34:35], v[34:35], 0, s[8:9]
	global_load_dwordx2 v[48:49], v[36:37], off
	global_load_dwordx2 v[46:47], v[36:37], off offset:512
	global_load_dwordx2 v[44:45], v[36:37], off offset:1024
	global_load_dwordx2 v[42:43], v[36:37], off offset:1536
	global_load_dwordx2 v[40:41], v[34:35], off
	global_load_dwordx2 v[38:39], v[34:35], off offset:512
	s_nop 0
	global_load_dwordx2 v[36:37], v[34:35], off offset:1024
	s_nop 0
	global_load_dwordx2 v[34:35], v[34:35], off offset:1536
	s_waitcnt vmcnt(31)
	v_pk_add_f32 v[148:149], v[148:149], 1.0 op_sel_hi:[1,0]
	v_pk_add_f32 v[146:147], v[146:147], 1.0 op_sel_hi:[1,0]
	v_pk_mul_f32 v[18:19], v[144:145], v[148:149]
	v_pk_mul_f32 v[20:21], v[142:143], v[146:147]
	v_pk_add_f32 v[156:157], v[156:157], 1.0 op_sel_hi:[1,0]
	v_pk_add_f32 v[154:155], v[154:155], 1.0 op_sel_hi:[1,0]
	v_pk_mul_f32 v[22:23], v[152:153], v[156:157]
	v_pk_mul_f32 v[24:25], v[150:151], v[154:155]
	v_pk_add_f32 v[164:165], v[164:165], 1.0 op_sel_hi:[1,0]
	v_pk_add_f32 v[162:163], v[162:163], 1.0 op_sel_hi:[1,0]
	v_pk_mul_f32 v[26:27], v[160:161], v[164:165]
	v_pk_mul_f32 v[28:29], v[158:159], v[162:163]
	v_pk_add_f32 v[172:173], v[172:173], 1.0 op_sel_hi:[1,0]
	v_pk_add_f32 v[170:171], v[170:171], 1.0 op_sel_hi:[1,0]
	v_pk_mul_f32 v[30:31], v[168:169], v[172:173]
	v_pk_mul_f32 v[32:33], v[166:167], v[170:171]
	v_lshlrev_b32_e32 v98, 16, v94
	v_and_b32_e32 v99, 0xffff0000, v94
	v_lshlrev_b32_e32 v94, 16, v95
	v_and_b32_e32 v95, 0xffff0000, v95
	s_waitcnt vmcnt(29)
	v_lshlrev_b32_e32 v102, 16, v92
	v_and_b32_e32 v103, 0xffff0000, v92
	v_lshlrev_b32_e32 v104, 16, v93
	v_and_b32_e32 v105, 0xffff0000, v93
	v_mul_f32_e32 v92, v99, v99
	v_mul_f32_e32 v93, v95, v95
	v_lshlrev_b32_e32 v100, 16, v90
	v_and_b32_e32 v101, 0xffff0000, v90
	v_lshlrev_b32_e32 v90, 16, v91
	v_and_b32_e32 v91, 0xffff0000, v91
	v_fmac_f32_e32 v92, v98, v98
	v_fmac_f32_e32 v93, v94, v94
	s_waitcnt vmcnt(28)
	v_lshlrev_b32_e32 v106, 16, v96
	v_and_b32_e32 v107, 0xffff0000, v96
	v_add_f32_e32 v92, v92, v93
	v_mul_f32_e32 v93, v101, v101
	v_mul_f32_e32 v96, v91, v91
	v_fmac_f32_e32 v93, v100, v100
	v_fmac_f32_e32 v96, v90, v90
	v_add_f32_e32 v93, v93, v96
	v_add_f32_e32 v92, v92, v93
	v_mul_f32_e32 v93, v103, v103
	v_mul_f32_e32 v96, v105, v105
	v_fmac_f32_e32 v93, v102, v102
	v_fmac_f32_e32 v96, v104, v104
	v_and_b32_e32 v109, 0xffff0000, v97
	v_add_f32_e32 v93, v93, v96
	v_lshlrev_b32_e32 v108, 16, v97
	v_add_f32_e32 v92, v92, v93
	v_mul_f32_e32 v93, v107, v107
	v_mul_f32_e32 v96, v109, v109
	v_fmac_f32_e32 v93, v106, v106
	v_fmac_f32_e32 v96, v108, v108
	v_add_f32_e32 v93, v93, v96
	v_add_f32_e32 v92, v92, v93
	v_mov_b32_e32 v93, v1
	s_nop 0
	v_add_f32_dpp v92, v92, v92 quad_perm:[1,0,3,2] row_mask:0xf bank_mask:0xf bound_ctrl:1
	s_nop 1
	v_add_f32_dpp v92, v92, v92 quad_perm:[2,3,0,1] row_mask:0xf bank_mask:0xf bound_ctrl:1
	s_nop 1
	v_add_f32_dpp v92, v92, v92 row_ror:4 row_mask:0xf bank_mask:0xf bound_ctrl:1
	s_nop 1
	v_add_f32_dpp v92, v92, v92 row_ror:8 row_mask:0xf bank_mask:0xf bound_ctrl:1
	s_nop 1
	v_mov_b32_dpp v93, v92 row_bcast:15 row_mask:0xa bank_mask:0xf
	v_add_f32_e32 v92, v92, v93
	v_mov_b32_e32 v93, v1
	s_nop 1
	v_mov_b32_dpp v93, v92 row_bcast:31 row_mask:0xc bank_mask:0xf
	v_add_f32_e32 v92, v92, v93
	s_nop 0
	v_readlane_b32 s8, v92, 63
	s_nop 1
	v_fma_f32 v92, s8, v236, v232
	v_cmp_gt_f32_e32 vcc, s84, v92
	v_mul_f32_e32 v93, 0x4f800000, v92
	s_nop 0
	v_cndmask_b32_e32 v92, v92, v93, vcc
	v_sqrt_f32_e32 v93, v92
	s_nop 0
	v_add_u32_e32 v96, -1, v93
	v_fma_f32 v97, -v96, v93, v92
	v_cmp_ge_f32_e64 s[8:9], 0, v97
	v_add_u32_e32 v97, 1, v93
	s_nop 0
	v_cndmask_b32_e64 v96, v93, v96, s[8:9]
	v_fma_f32 v93, -v97, v93, v92
	v_cmp_lt_f32_e64 s[8:9], 0, v93
	s_nop 1
	v_cndmask_b32_e64 v93, v96, v97, s[8:9]
	v_mul_f32_e32 v96, 0x37800000, v93
	v_cndmask_b32_e32 v93, v93, v96, vcc
	v_cmp_class_f32_e32 vcc, v92, v233
	s_nop 1
	v_cndmask_b32_e32 v92, v93, v92, vcc
	v_div_scale_f32 v93, s[8:9], v92, v92, 1.0
	v_rcp_f32_e32 v96, v93
	s_nop 0
	v_fma_f32 v97, -v93, v96, 1.0
	v_fmac_f32_e32 v96, v97, v96
	v_div_scale_f32 v97, vcc, 1.0, v92, 1.0
	v_mul_f32_e32 v110, v97, v96
	v_fma_f32 v111, -v93, v110, v97
	v_fmac_f32_e32 v110, v111, v96
	v_fma_f32 v93, -v93, v110, v97
	v_div_fmas_f32 v93, v93, v96, v110
	v_div_fixup_f32 v110, v93, v92, 1.0
	v_pk_mul_f32 v[92:93], v[94:95], v[110:111] op_sel_hi:[1,0]
	v_pk_mul_f32 v[96:97], v[98:99], v[110:111] op_sel_hi:[1,0]
	v_pk_fma_f32 v[92:93], v[18:19], v[92:93], v[4:5]
	v_pk_fma_f32 v[96:97], v[20:21], v[96:97], v[2:3]
	v_max_f32_e64 v94, |v92|, |v93|
	v_max3_f32 v111, |v96|, |v97|, v94
	v_pk_mul_f32 v[90:91], v[90:91], v[110:111] op_sel_hi:[1,0]
	v_pk_mul_f32 v[98:99], v[100:101], v[110:111] op_sel_hi:[1,0]
	v_pk_fma_f32 v[94:95], v[22:23], v[90:91], v[8:9]
	v_pk_fma_f32 v[98:99], v[24:25], v[98:99], v[6:7]
	v_max_f32_e64 v90, |v94|, |v95|
	v_max3_f32 v90, |v98|, |v99|, v90
	v_max3_f32 v111, v111, 0, v90
	v_pk_mul_f32 v[100:101], v[104:105], v[110:111] op_sel_hi:[1,0]
	v_pk_mul_f32 v[90:91], v[102:103], v[110:111] op_sel_hi:[1,0]
	v_pk_fma_f32 v[100:101], v[26:27], v[100:101], v[12:13]
	v_pk_fma_f32 v[102:103], v[28:29], v[90:91], v[10:11]
	v_max_f32_e64 v90, |v100|, |v101|
	v_max3_f32 v112, |v102|, |v103|, v90
	v_pk_mul_f32 v[90:91], v[108:109], v[110:111] op_sel_hi:[1,0]
	v_pk_mul_f32 v[104:105], v[106:107], v[110:111] op_sel_hi:[1,0]
	v_pk_fma_f32 v[90:91], v[30:31], v[90:91], v[16:17]
	v_pk_fma_f32 v[104:105], v[32:33], v[104:105], v[14:15]
	v_max_f32_e64 v106, |v90|, |v91|
	v_max3_f32 v106, |v104|, |v105|, v106
	v_max3_f32 v106, v111, v112, v106
	v_mov_b32_e32 v107, v106
	s_nop 1
	v_mov_b32_dpp v107, v107 quad_perm:[1,0,3,2] row_mask:0xf bank_mask:0xf
	v_max_f32_e32 v107, v107, v107
	v_max_f32_e32 v106, v106, v107
	v_mov_b32_e32 v107, v106
	s_nop 1
	v_mov_b32_dpp v107, v107 quad_perm:[2,3,0,1] row_mask:0xf bank_mask:0xf
	v_max_f32_e32 v107, v107, v107
	v_max_f32_e32 v106, v106, v107
	v_mov_b32_e32 v107, v106
	s_nop 1
	v_mov_b32_dpp v107, v107 row_ror:4 row_mask:0xf bank_mask:0xf
	v_max_f32_e32 v107, v107, v107
	v_max_f32_e32 v106, v106, v107
	v_mov_b32_e32 v107, v106
	s_nop 1
	v_mov_b32_dpp v107, v107 row_ror:8 row_mask:0xf bank_mask:0xf
	v_max_f32_e32 v107, v107, v107
	v_max_f32_e32 v106, v106, v107
	v_mov_b32_e32 v107, v106
	s_nop 1
	v_mov_b32_dpp v107, v107 row_bcast:15 row_mask:0xa bank_mask:0xf
	v_max_f32_e32 v107, v107, v107
	v_max_f32_e32 v106, v106, v107
	v_mov_b32_e32 v107, v106
	s_nop 1
	v_mov_b32_dpp v107, v107 row_bcast:31 row_mask:0xc bank_mask:0xf
	v_max_f32_e32 v107, v107, v107
	v_max_f32_e32 v106, v106, v107
	s_nop 0
	v_readlane_b32 s26, v106, 63
	s_nop 1
	v_cmp_gt_f32_e64 s[8:9], s26, 0
	s_and_saveexec_b64 s[24:25], s[6:7]
	s_cbranch_execz .LBB0_636
	s_lshl_b64 s[28:29], s[22:23], 2
	v_mul_f32_e32 v106, s26, v237
	s_add_u32 s28, s37, s28
	v_cndmask_b32_e64 v106, 1.0, v106, s[8:9]
	s_addc_u32 s29, s38, s29
	global_store_dword v1, v106, s[28:29]

.LBB0_652:
	s_add_u32 s16, s0, 0x680000
	s_addc_u32 s17, s1, 0
	s_load_dwordx2 s[4:5], s[2:3], 0x0
	s_load_dwordx2 s[8:9], s[2:3], 0x28
	s_lshl_b32 s18, s36, 6
	v_readlane_b32 s2, v254, 9
	s_add_i32 s18, s18, s2
	s_ashr_i32 s2, s18, 11
	s_mul_hi_i32 s3, s2, 0x6000
	s_mulk_i32 s2, 0x6000
	s_waitcnt vmcnt(0)
	v_mbcnt_lo_u32_b32 v0, -1, 0
	v_mbcnt_hi_u32_b32 v0, -1, v0
	s_add_u32 s2, s34, s2
	v_and_b32_e32 v0, 63, v0
	s_addc_u32 s3, s35, s3
	s_add_u32 s6, s2, 0x1000
	v_lshlrev_b32_e32 v24, 4, v0
	s_addc_u32 s7, s3, 0
	s_waitcnt lgkmcnt(0)
	global_load_dwordx4 v[142:145], v24, s[8:9]
	global_load_dwordx4 v[146:149], v24, s[6:7]
	v_or_b32_e32 v10, 0x400, v24
	v_or_b32_e32 v14, 0x800, v24
	v_or_b32_e32 v18, 0xc00, v24
	v_lshlrev_b32_e32 v22, 2, v0
	v_mov_b32_e32 v23, v1
	v_mov_b32_e32 v25, v1
	v_lshl_add_u64 v[98:99], s[4:5], 0, v[24:25]
	global_load_dwordx4 v[2:5], v24, s[2:3]
	global_load_dwordx4 v[150:153], v24, s[8:9] offset:1024
	s_nop 0
	global_load_dwordx4 v[154:157], v10, s[6:7]
	global_load_dwordx4 v[6:9], v24, s[2:3] offset:1024
	global_load_dwordx4 v[158:161], v24, s[8:9] offset:2048
	s_nop 0
	global_load_dwordx4 v[162:165], v14, s[6:7]
	global_load_dwordx4 v[166:169], v24, s[8:9] offset:3072
	s_nop 0
	global_load_dwordx4 v[170:173], v18, s[6:7]
	global_load_dwordx4 v[10:13], v24, s[2:3] offset:2048
	global_load_dwordx4 v[14:17], v24, s[2:3] offset:3072
	v_cmp_eq_u32_e64 s[6:7], 0, v0
	s_waitcnt vmcnt(0)
	v_pk_add_f32 v[148:149], v[148:149], 1.0 op_sel_hi:[1,0]
	v_pk_add_f32 v[146:147], v[146:147], 1.0 op_sel_hi:[1,0]
	v_pk_mul_f32 v[82:83], v[144:145], v[148:149]
	v_pk_mul_f32 v[84:85], v[142:143], v[146:147]
	v_pk_add_f32 v[156:157], v[156:157], 1.0 op_sel_hi:[1,0]
	v_pk_add_f32 v[154:155], v[154:155], 1.0 op_sel_hi:[1,0]
	v_pk_mul_f32 v[86:87], v[152:153], v[156:157]
	v_pk_mul_f32 v[88:89], v[150:151], v[154:155]
	v_pk_add_f32 v[164:165], v[164:165], 1.0 op_sel_hi:[1,0]
	v_pk_add_f32 v[162:163], v[162:163], 1.0 op_sel_hi:[1,0]
	v_pk_mul_f32 v[90:91], v[160:161], v[164:165]
	v_pk_mul_f32 v[92:93], v[158:159], v[162:163]
	v_pk_add_f32 v[172:173], v[172:173], 1.0 op_sel_hi:[1,0]
	v_pk_add_f32 v[170:171], v[170:171], 1.0 op_sel_hi:[1,0]
	v_pk_mul_f32 v[94:95], v[168:169], v[172:173]
	v_pk_mul_f32 v[96:97], v[166:167], v[170:171]
	v_lshl_add_u64 v[18:19], s[0:1], 0, v[22:23]
	s_mov_b64 s[0:1], 0x15000000
	s_mov_b32 s2, 0
	v_lshl_add_u64 v[100:101], v[18:19], 0, s[0:1]
	s_mov_b64 s[0:1], -1
	s_branch .LBB0_654

.LBB0_1390:
.LBB0_1391:
	s_cmp_le_i32 s93, s30
	s_cselect_b64 s[2:3], -1, 0
	s_and_b64 s[0:1], s[2:3], s[0:1]
	s_and_b64 s[0:1], s[0:1], s[26:27]
	s_andn2_b64 vcc, exec, s[0:1]
	s_cbranch_vccnz .LBB0_1398
	s_mov_b64 s[2:3], s[96:97]
	v_readlane_b32 s4, v254, 30
	v_readlane_b32 s5, v254, 31
	s_lshl_b32 s94, s47, 6
	v_readlane_b32 s4, v254, 0
	v_readlane_b32 s5, v254, 1
	s_mov_b32 s8, s4
	s_lshl_b64 s[4:5], s[94:95], 2
	v_readlane_b32 s6, v254, 39
	s_add_u32 s6, s6, s4
	v_readlane_b32 s4, v254, 40
	s_addc_u32 s7, s4, s5
	s_load_dwordx2 s[2:3], s[2:3], 0xc8
	s_waitcnt vmcnt(59)
	v_mbcnt_lo_u32_b32 v31, -1, 0
	v_mbcnt_hi_u32_b32 v31, -1, v31
	global_load_dword v33, v1, s[6:7] sc1
	global_load_dword v37, v1, s[6:7] offset:4 sc1
	global_load_dword v41, v1, s[6:7] offset:8 sc1
	global_load_dword v43, v1, s[6:7] offset:12 sc1
	global_load_dword v45, v1, s[6:7] offset:16 sc1
	global_load_dword v35, v1, s[6:7] offset:20 sc1
	global_load_dword v39, v1, s[6:7] offset:24 sc1
	global_load_dword v0, v1, s[6:7] offset:28 sc1
	s_cmp_eq_u32 s8, 0
	v_or_b32_e32 v2, s73, v31
	s_cselect_b64 s[4:5], -1, 0
	s_waitcnt vmcnt(1)
	v_add_u32_e32 v33, 0xff, v33
	v_and_b32_e32 v33, 0xffffff00, v33
	v_add_u32_e32 v37, 0xff, v37
	v_and_b32_e32 v37, 0xffffff00, v37
	v_add_u32_e32 v37, v37, v33
	v_add_u32_e32 v41, 0xff, v41
	v_and_b32_e32 v41, 0xffffff00, v41
	v_add_u32_e32 v41, v41, v37
	v_add_u32_e32 v43, 0xff, v43
	v_and_b32_e32 v43, 0xffffff00, v43
	v_add_u32_e32 v43, v43, v41
	v_add_u32_e32 v45, 0xff, v45
	v_and_b32_e32 v45, 0xffffff00, v45
	v_add_u32_e32 v45, v45, v43
	v_add_u32_e32 v35, 0xff, v35
	v_and_b32_e32 v35, 0xffffff00, v35
	v_add_u32_e32 v35, v35, v45
	v_add_u32_e32 v39, 0xff, v39
	v_and_b32_e32 v39, 0xffffff00, v39
	v_add_u32_e32 v39, v39, v35
	s_movk_i32 s6, 0xa0
	v_cmp_gt_i32_e32 vcc, s6, v2
	s_and_b64 s[6:7], s[4:5], vcc
	s_and_saveexec_b64 s[4:5], s[6:7]
	s_cbranch_execz .LBB0_1395
	v_lshlrev_b32_e32 v3, 8, v2
	v_cmp_ge_i32_e32 vcc, v3, v33
	s_nop 1
	v_cndmask_b32_e64 v4, 0, 1, vcc
	v_cmp_ge_i32_e32 vcc, v3, v37
	s_nop 1
	v_cndmask_b32_e64 v5, 0, 1, vcc
	v_cmp_ge_i32_e32 vcc, v3, v41
	s_nop 1
	v_addc_co_u32_e32 v4, vcc, v5, v4, vcc
	v_cmp_ge_i32_e32 vcc, v3, v43
	s_nop 1
	v_cndmask_b32_e64 v5, 0, 1, vcc
	v_cmp_ge_i32_e32 vcc, v3, v45
	s_nop 1
	v_addc_co_u32_e32 v4, vcc, v4, v5, vcc
	v_cmp_ge_i32_e32 vcc, v3, v35
	s_nop 1
	v_cndmask_b32_e64 v5, 0, 1, vcc
	v_cmp_ge_i32_e32 vcc, v3, v39
	v_ashrrev_i32_e32 v3, 31, v2
	s_nop 0
	v_addc_co_u32_e32 v6, vcc, v4, v5, vcc
	s_waitcnt lgkmcnt(0)
	v_lshl_add_u64 v[4:5], v[2:3], 2, s[2:3]
	v_add_co_u32_e32 v4, vcc, 0x781000, v4
	s_nop 1
	v_addc_co_u32_e32 v5, vcc, 0, v5, vcc
	v_cmp_eq_u32_e32 vcc, 0, v2
	global_store_dword v[4:5], v6, off
	s_and_b64 exec, exec, vcc
	s_cbranch_execz .LBB0_1395
	s_waitcnt vmcnt(1)
	v_add_u32_e32 v0, 0xff, v0
	v_and_b32_e32 v0, 0xffffff00, v0
	v_add_u32_e32 v0, v0, v39
	v_ashrrev_i32_e32 v0, 8, v0
	global_store_dword v239, v0, s[2:3] offset:640
